# v27 + P8 epilogue: relu/square/clamp as med3(t,0,sqrt448)+square (identical fp8 outputs), one VALU fewer per element
# speedup vs baseline: 1.0037x; 1.0037x over previous
; __device__ __forceinline__ unsigned pk4_fp8(float a, float b, float c, float d) {
;     a = fminf(fmaxf(a, -448.f), 448.f); b = fminf(fmaxf(b, -448.f), 448.f); c = fminf(fmaxf(c, -448.f), 448.f); d = fminf(fmaxf(d, -448.f), 448.f);
;     int w = 0; w = __builtin_amdgcn_cvt_pk_fp8_f32(a, b, w, false); w = __builtin_amdgcn_cvt_pk_fp8_f32(c, d, w, true); return (unsigned)w;
;     __device__ __forceinline__ void operator()(const f32x4 (&acc)[2][2][4][2], const Unit& u, int wr, int wc, int fr, int fq) const {
;     ...
;                 const int row = row0 + ai * HALF + m * 16;
;                 const float rs = rsqrtf(ss[row] * (1.0f / 4096.0f) + RMS_EPS) * (1.0f / 64.0f);
;                 unsigned char* rowp = U + ((size_t)(row >> 4) * 512 + (col0 >> 5)) * 512 + (row & 15) * 32 + (col0 & 31);
; #pragma unroll
;                 for (int bj = 0; bj < 2; ++bj) {
;                     f32x4 v0 = acc[ai][bj][m][0] * rs, v1 = acc[ai][bj][m][1] * rs;
; #pragma unroll
;                     for (int j = 0; j < 4; ++j) { const float a = fmaxf(v0[j], 0.f), b = fmaxf(v1[j], 0.f); v0[j] = a * a * 4.f; v1[j] = b * b * 4.f; }
;                     u32x2 w; w.x = pk4_fp8(v0[0], v0[1], v0[2], v0[3]); w.y = pk4_fp8(v1[0], v1[1], v1[2], v1[3]);
;                     *(u32x2*)(rowp + bj * (HALF / 32) * 512) = w;
.LBB0_2284:
	s_mov_b32 s99, 0x41a953fd
	s_lshl_b32 s13, s20, 8
	s_add_i32 s13, s13, s36
	v_or_b32_e32 v2, s13, v1
	v_ashrrev_i32_e32 v3, 31, v2
	s_nop 15
	s_nop 15
	v_lshl_add_u64 v[4:5], v[2:3], 2, s[2:3]
	s_lshl_b32 s15, s21, 8
	s_or_b32 s15, s15, s37
	v_mov_b32_e32 v6, 0
	v_mov_b32_e32 v7, 0
	s_ashr_i32 s20, s15, 5
	s_ashr_i32 s22, s13, 4
	v_mov_b32_e32 v8, 0
	s_ashr_i32 s21, s20, 31
	s_ashr_i32 s23, s22, 31
	s_lshl_b64 s[20:21], s[20:21], 9
	s_lshl_b64 s[22:23], s[22:23], 18
	v_readlane_b32 s24, v253, 46
	v_readlane_b32 s25, v253, 47
	s_add_u32 s13, s24, s22
	s_addc_u32 s15, s25, s23
	s_add_u32 s22, s13, s20
	s_addc_u32 s23, s15, s21
	s_waitcnt vmcnt(0)
	v_fmamk_f32 v3, v234, 0x39800000, v194
	v_mul_f32_e32 v9, 0x4b800000, v3
	v_cmp_gt_f32_e32 vcc, s43, v3
	s_nop 1
	v_cndmask_b32_e32 v3, v3, v9, vcc
	v_rsq_f32_e32 v3, v3
	s_nop 0
	v_mul_f32_e32 v9, 0x45800000, v3
	v_cndmask_b32_e32 v3, v3, v9, vcc
	v_mul_f32_e32 v10, 0x3d000000, v3
	v_pk_mul_f32 v[14:15], v[158:159], v[10:11] op_sel_hi:[1,0]
	v_pk_mul_f32 v[18:19], v[154:155], v[10:11] op_sel_hi:[1,0]
	v_pk_mul_f32 v[12:13], v[160:161], v[10:11] op_sel_hi:[1,0]
	v_pk_mul_f32 v[16:17], v[156:157], v[10:11] op_sel_hi:[1,0]
	v_pk_mul_f32 v[20:21], v[152:153], v[10:11] op_sel_hi:[1,0]
	v_pk_mul_f32 v[22:23], v[150:151], v[10:11] op_sel_hi:[1,0]
	v_pk_mul_f32 v[24:25], v[148:149], v[10:11] op_sel_hi:[1,0]
	v_pk_mul_f32 v[10:11], v[146:147], v[10:11] op_sel_hi:[1,0]
	v_med3_f32 v3, v14, 0, s99
	v_med3_f32 v9, v18, 0, s99
	v_med3_f32 v14, v15, 0, s99
	v_med3_f32 v15, v19, 0, s99
	v_med3_f32 v18, v22, 0, s99
	v_med3_f32 v10, v10, 0, s99
	v_med3_f32 v19, v23, 0, s99
	v_med3_f32 v11, v11, 0, s99
	v_mul_f32_e32 v3, v3, v3
	v_mul_f32_e32 v9, v9, v9
	v_mul_f32_e32 v14, v14, v14
	v_mul_f32_e32 v15, v15, v15
	v_mul_f32_e32 v18, v18, v18
	v_mul_f32_e32 v10, v10, v10
	v_mul_f32_e32 v19, v19, v19
	v_mul_f32_e32 v11, v11, v11
	v_med3_f32 v12, v12, 0, s99
	v_med3_f32 v16, v16, 0, s99
	v_med3_f32 v13, v13, 0, s99
	v_med3_f32 v17, v17, 0, s99
	v_cvt_pk_fp8_f32 v6, v3, v14
	v_cvt_pk_fp8_f32 v7, v9, v15
	v_mov_b32_e32 v3, v11
	v_mov_b32_e32 v9, 0
	v_med3_f32 v20, v20, 0, s99
	v_med3_f32 v22, v24, 0, s99
	v_med3_f32 v21, v21, 0, s99
	v_med3_f32 v23, v25, 0, s99
	v_mul_f32_e32 v12, v12, v12
	v_mul_f32_e32 v16, v16, v16
	v_mul_f32_e32 v13, v13, v13
	v_mul_f32_e32 v17, v17, v17
	v_cvt_pk_fp8_f32 v8, v18, v19
	v_cvt_pk_fp8_f32 v9, v10, v3
	v_mul_f32_e32 v20, v20, v20
	v_mul_f32_e32 v22, v22, v22
	v_mul_f32_e32 v21, v21, v21
	v_mul_f32_e32 v23, v23, v23
	v_cvt_pk_fp8_f32 v6, v12, v13 op_sel:[0,0,1]
	v_cvt_pk_fp8_f32 v7, v16, v17 op_sel:[0,0,1]
	v_mov_b32_e32 v3, v22
	v_mov_b32_e32 v10, v23
	v_cvt_pk_fp8_f32 v8, v20, v21 op_sel:[0,0,1]
	v_cvt_pk_fp8_f32 v9, v3, v10 op_sel:[0,0,1]
	v_lshl_add_u64 v[10:11], s[22:23], 0, v[172:173]
	v_lshl_add_u64 v[10:11], v[10:11], 0, v[170:171]
	global_store_dwordx2 v[10:11], v[6:7], off
	global_store_dwordx2 v[10:11], v[8:9], off offset:2048
	v_or_b32_e32 v6, 16, v2
	v_ashrrev_i32_e32 v7, 31, v6
	v_lshl_add_u64 v[8:9], v[6:7], 2, s[2:3]
	v_mov_b32_e32 v8, 0
	v_mov_b32_e32 v9, 0
	v_mov_b32_e32 v10, 0
	v_ashrrev_i32_e32 v6, 4, v6
	v_ashrrev_i32_e32 v7, 31, v6
	v_lshlrev_b64 v[6:7], 18, v[6:7]
	v_lshl_add_u64 v[6:7], s[24:25], 0, v[6:7]
	v_lshl_add_u64 v[6:7], v[6:7], 0, s[20:21]
	v_lshl_add_u64 v[6:7], v[6:7], 0, v[172:173]
	v_lshl_add_u64 v[6:7], v[6:7], 0, v[170:171]
	v_fmamk_f32 v3, v235, 0x39800000, v194
	v_mul_f32_e32 v11, 0x4b800000, v3
	v_cmp_gt_f32_e32 vcc, s43, v3
	s_nop 1
	v_cndmask_b32_e32 v3, v3, v11, vcc
	v_rsq_f32_e32 v3, v3
	s_nop 0
	v_mul_f32_e32 v11, 0x45800000, v3
	v_cndmask_b32_e32 v3, v3, v11, vcc
	v_mul_f32_e32 v12, 0x3d000000, v3
	v_pk_mul_f32 v[16:17], v[142:143], v[12:13] op_sel_hi:[1,0]
	v_pk_mul_f32 v[20:21], v[138:139], v[12:13] op_sel_hi:[1,0]
	v_pk_mul_f32 v[14:15], v[144:145], v[12:13] op_sel_hi:[1,0]
	v_pk_mul_f32 v[18:19], v[140:141], v[12:13] op_sel_hi:[1,0]
	v_pk_mul_f32 v[22:23], v[136:137], v[12:13] op_sel_hi:[1,0]
	v_pk_mul_f32 v[24:25], v[134:135], v[12:13] op_sel_hi:[1,0]
	v_pk_mul_f32 v[26:27], v[132:133], v[12:13] op_sel_hi:[1,0]
	v_pk_mul_f32 v[12:13], v[130:131], v[12:13] op_sel_hi:[1,0]
	v_med3_f32 v3, v16, 0, s99
	v_med3_f32 v11, v20, 0, s99
	v_med3_f32 v16, v17, 0, s99
	v_med3_f32 v17, v21, 0, s99
	v_med3_f32 v20, v24, 0, s99
	v_med3_f32 v12, v12, 0, s99
	v_med3_f32 v21, v25, 0, s99
	v_med3_f32 v13, v13, 0, s99
	v_mul_f32_e32 v3, v3, v3
	v_mul_f32_e32 v11, v11, v11
	v_mul_f32_e32 v16, v16, v16
	v_mul_f32_e32 v17, v17, v17
	v_mul_f32_e32 v20, v20, v20
	v_mul_f32_e32 v12, v12, v12
	v_mul_f32_e32 v21, v21, v21
	v_mul_f32_e32 v13, v13, v13
	v_med3_f32 v14, v14, 0, s99
	v_med3_f32 v18, v18, 0, s99
	v_med3_f32 v15, v15, 0, s99
	v_med3_f32 v19, v19, 0, s99
	v_cvt_pk_fp8_f32 v8, v3, v16
	v_cvt_pk_fp8_f32 v9, v11, v17
	v_mov_b32_e32 v3, v12
	v_mov_b32_e32 v12, v13
	v_mov_b32_e32 v11, 0
	v_med3_f32 v22, v22, 0, s99
	v_med3_f32 v24, v26, 0, s99
	v_med3_f32 v23, v23, 0, s99
	v_med3_f32 v25, v27, 0, s99
	v_mul_f32_e32 v14, v14, v14
	v_mul_f32_e32 v18, v18, v18
	v_mul_f32_e32 v15, v15, v15
	v_mul_f32_e32 v19, v19, v19
	v_cvt_pk_fp8_f32 v10, v20, v21
	v_cvt_pk_fp8_f32 v11, v3, v12
	v_mul_f32_e32 v22, v22, v22
	v_mul_f32_e32 v24, v24, v24
	v_mul_f32_e32 v23, v23, v23
	v_mul_f32_e32 v25, v25, v25
	v_cvt_pk_fp8_f32 v8, v14, v15 op_sel:[0,0,1]
	v_cvt_pk_fp8_f32 v9, v18, v19 op_sel:[0,0,1]
	v_mov_b32_e32 v3, v24
	v_mov_b32_e32 v12, v25
	v_cvt_pk_fp8_f32 v10, v22, v23 op_sel:[0,0,1]
	v_cvt_pk_fp8_f32 v11, v3, v12 op_sel:[0,0,1]
	global_store_dwordx2 v[6:7], v[8:9], off
	global_store_dwordx2 v[6:7], v[10:11], off offset:2048
	v_or_b32_e32 v6, 32, v2
; __device__ __forceinline__ unsigned pk4_fp8(float a, float b, float c, float d) {
;     a = fminf(fmaxf(a, -448.f), 448.f); b = fminf(fmaxf(b, -448.f), 448.f); c = fminf(fmaxf(c, -448.f), 448.f); d = fminf(fmaxf(d, -448.f), 448.f);
;     int w = 0; w = __builtin_amdgcn_cvt_pk_fp8_f32(a, b, w, false); w = __builtin_amdgcn_cvt_pk_fp8_f32(c, d, w, true); return (unsigned)w;
;     __device__ __forceinline__ void operator()(const f32x4 (&acc)[2][2][4][2], const Unit& u, int wr, int wc, int fr, int fq) const {
;     ...
;                 const int row = row0 + ai * HALF + m * 16;
;                 const float rs = rsqrtf(ss[row] * (1.0f / 4096.0f) + RMS_EPS) * (1.0f / 64.0f);
;                 unsigned char* rowp = U + ((size_t)(row >> 4) * 512 + (col0 >> 5)) * 512 + (row & 15) * 32 + (col0 & 31);
; #pragma unroll
;                 for (int bj = 0; bj < 2; ++bj) {
;                     f32x4 v0 = acc[ai][bj][m][0] * rs, v1 = acc[ai][bj][m][1] * rs;
; #pragma unroll
;                     for (int j = 0; j < 4; ++j) { const float a = fmaxf(v0[j], 0.f), b = fmaxf(v1[j], 0.f); v0[j] = a * a * 4.f; v1[j] = b * b * 4.f; }
;                     u32x2 w; w.x = pk4_fp8(v0[0], v0[1], v0[2], v0[3]); w.y = pk4_fp8(v1[0], v1[1], v1[2], v1[3]);
;                     *(u32x2*)(rowp + bj * (HALF / 32) * 512) = w;
	v_ashrrev_i32_e32 v7, 31, v6
	v_lshl_add_u64 v[8:9], v[6:7], 2, s[2:3]
	v_mov_b32_e32 v8, 0
	v_mov_b32_e32 v9, 0
	v_mov_b32_e32 v10, 0
	v_ashrrev_i32_e32 v6, 4, v6
	v_ashrrev_i32_e32 v7, 31, v6
	v_lshlrev_b64 v[6:7], 18, v[6:7]
	v_lshl_add_u64 v[6:7], s[24:25], 0, v[6:7]
	v_lshl_add_u64 v[6:7], v[6:7], 0, s[20:21]
	v_lshl_add_u64 v[6:7], v[6:7], 0, v[172:173]
	v_lshl_add_u64 v[6:7], v[6:7], 0, v[170:171]
	v_fmamk_f32 v3, v236, 0x39800000, v194
	v_mul_f32_e32 v11, 0x4b800000, v3
	v_cmp_gt_f32_e32 vcc, s43, v3
	s_nop 1
	v_cndmask_b32_e32 v3, v3, v11, vcc
	v_rsq_f32_e32 v3, v3
	s_nop 0
	v_mul_f32_e32 v11, 0x45800000, v3
	v_cndmask_b32_e32 v3, v3, v11, vcc
	v_mul_f32_e32 v12, 0x3d000000, v3
	v_pk_mul_f32 v[16:17], v[126:127], v[12:13] op_sel_hi:[1,0]
	v_pk_mul_f32 v[20:21], v[122:123], v[12:13] op_sel_hi:[1,0]
	v_pk_mul_f32 v[24:25], v[118:119], v[12:13] op_sel_hi:[1,0]
	v_pk_mul_f32 v[14:15], v[128:129], v[12:13] op_sel_hi:[1,0]
	v_pk_mul_f32 v[18:19], v[124:125], v[12:13] op_sel_hi:[1,0]
	v_pk_mul_f32 v[22:23], v[120:121], v[12:13] op_sel_hi:[1,0]
	v_pk_mul_f32 v[26:27], v[116:117], v[12:13] op_sel_hi:[1,0]
	v_pk_mul_f32 v[12:13], v[114:115], v[12:13] op_sel_hi:[1,0]
	v_med3_f32 v3, v16, 0, s99
	v_med3_f32 v11, v20, 0, s99
	v_med3_f32 v16, v17, 0, s99
	v_med3_f32 v17, v21, 0, s99
	v_med3_f32 v20, v24, 0, s99
	v_med3_f32 v21, v25, 0, s99
	v_med3_f32 v12, v12, 0, s99
	v_med3_f32 v13, v13, 0, s99
	v_mul_f32_e32 v3, v3, v3
	v_mul_f32_e32 v11, v11, v11
	v_mul_f32_e32 v16, v16, v16
	v_mul_f32_e32 v17, v17, v17
	v_mul_f32_e32 v20, v20, v20
	v_mul_f32_e32 v21, v21, v21
	v_mul_f32_e32 v12, v12, v12
	v_mul_f32_e32 v13, v13, v13
	v_med3_f32 v14, v14, 0, s99
	v_med3_f32 v18, v18, 0, s99
	v_med3_f32 v15, v15, 0, s99
	v_med3_f32 v19, v19, 0, s99
	v_med3_f32 v22, v22, 0, s99
	v_med3_f32 v23, v23, 0, s99
	v_cvt_pk_fp8_f32 v8, v3, v16
	v_cvt_pk_fp8_f32 v9, v11, v17
	v_cvt_pk_fp8_f32 v10, v20, v21
	v_mov_b32_e32 v11, 0
	v_med3_f32 v24, v26, 0, s99
	v_med3_f32 v25, v27, 0, s99
	v_mul_f32_e32 v14, v14, v14
	v_mul_f32_e32 v18, v18, v18
	v_mul_f32_e32 v15, v15, v15
	v_mul_f32_e32 v19, v19, v19
	v_mul_f32_e32 v22, v22, v22
	v_mul_f32_e32 v23, v23, v23
	v_cvt_pk_fp8_f32 v11, v12, v13
	v_mul_f32_e32 v24, v24, v24
	v_mul_f32_e32 v25, v25, v25
	v_mov_b32_e32 v3, v23
	v_cvt_pk_fp8_f32 v8, v14, v15 op_sel:[0,0,1]
	v_cvt_pk_fp8_f32 v9, v18, v19 op_sel:[0,0,1]
	v_cvt_pk_fp8_f32 v10, v22, v3 op_sel:[0,0,1]
	v_mov_b32_e32 v3, v24
	v_mov_b32_e32 v12, v25
	v_cvt_pk_fp8_f32 v11, v3, v12 op_sel:[0,0,1]
	global_store_dwordx2 v[6:7], v[8:9], off
	global_store_dwordx2 v[6:7], v[10:11], off offset:2048
	v_or_b32_e32 v6, 48, v2
	v_ashrrev_i32_e32 v7, 31, v6
	v_lshl_add_u64 v[8:9], v[6:7], 2, s[2:3]
	v_mov_b32_e32 v8, 0
	v_mov_b32_e32 v9, 0
	v_mov_b32_e32 v10, 0
	v_ashrrev_i32_e32 v6, 4, v6
	v_ashrrev_i32_e32 v7, 31, v6
	v_lshlrev_b64 v[6:7], 18, v[6:7]
	v_lshl_add_u64 v[6:7], s[24:25], 0, v[6:7]
	v_lshl_add_u64 v[6:7], v[6:7], 0, s[20:21]
	v_lshl_add_u64 v[6:7], v[6:7], 0, v[172:173]
	v_lshl_add_u64 v[6:7], v[6:7], 0, v[170:171]
	v_fmamk_f32 v3, v237, 0x39800000, v194
	v_mul_f32_e32 v11, 0x4b800000, v3
	v_cmp_gt_f32_e32 vcc, s43, v3
	s_nop 1
	v_cndmask_b32_e32 v3, v3, v11, vcc
	v_rsq_f32_e32 v3, v3
	s_nop 0
	v_mul_f32_e32 v11, 0x45800000, v3
	v_cndmask_b32_e32 v3, v3, v11, vcc
	v_mul_f32_e32 v12, 0x3d000000, v3
	v_pk_mul_f32 v[16:17], v[110:111], v[12:13] op_sel_hi:[1,0]
	v_pk_mul_f32 v[20:21], v[106:107], v[12:13] op_sel_hi:[1,0]
	v_pk_mul_f32 v[24:25], v[102:103], v[12:13] op_sel_hi:[1,0]
	v_pk_mul_f32 v[14:15], v[112:113], v[12:13] op_sel_hi:[1,0]
	v_pk_mul_f32 v[18:19], v[108:109], v[12:13] op_sel_hi:[1,0]
	v_pk_mul_f32 v[22:23], v[104:105], v[12:13] op_sel_hi:[1,0]
	v_pk_mul_f32 v[26:27], v[100:101], v[12:13] op_sel_hi:[1,0]
	v_pk_mul_f32 v[12:13], v[98:99], v[12:13] op_sel_hi:[1,0]
	v_med3_f32 v3, v16, 0, s99
	v_med3_f32 v11, v20, 0, s99
	v_med3_f32 v16, v17, 0, s99
	v_med3_f32 v17, v21, 0, s99
	v_med3_f32 v20, v24, 0, s99
	v_med3_f32 v21, v25, 0, s99
	v_med3_f32 v12, v12, 0, s99
	v_med3_f32 v13, v13, 0, s99
	v_mul_f32_e32 v3, v3, v3
	v_mul_f32_e32 v11, v11, v11
	v_mul_f32_e32 v16, v16, v16
	v_mul_f32_e32 v17, v17, v17
	v_mul_f32_e32 v20, v20, v20
	v_mul_f32_e32 v21, v21, v21
	v_mul_f32_e32 v12, v12, v12
	v_mul_f32_e32 v13, v13, v13
	v_med3_f32 v14, v14, 0, s99
	v_med3_f32 v18, v18, 0, s99
	v_med3_f32 v15, v15, 0, s99
	v_med3_f32 v19, v19, 0, s99
	v_med3_f32 v22, v22, 0, s99
	v_med3_f32 v23, v23, 0, s99
	v_cvt_pk_fp8_f32 v8, v3, v16
	v_cvt_pk_fp8_f32 v9, v11, v17
	v_cvt_pk_fp8_f32 v10, v20, v21
	v_mov_b32_e32 v11, 0
	v_med3_f32 v24, v26, 0, s99
	v_med3_f32 v25, v27, 0, s99
	v_mul_f32_e32 v14, v14, v14
	v_mul_f32_e32 v18, v18, v18
	v_mul_f32_e32 v15, v15, v15
	v_mul_f32_e32 v19, v19, v19
	v_mul_f32_e32 v22, v22, v22
	v_mul_f32_e32 v23, v23, v23
	v_cvt_pk_fp8_f32 v11, v12, v13
	v_mul_f32_e32 v24, v24, v24
	v_mul_f32_e32 v25, v25, v25
	v_mov_b32_e32 v3, v22
	v_mov_b32_e32 v16, v23
	v_cvt_pk_fp8_f32 v8, v14, v15 op_sel:[0,0,1]
	v_cvt_pk_fp8_f32 v9, v18, v19 op_sel:[0,0,1]
	v_cvt_pk_fp8_f32 v10, v3, v16 op_sel:[0,0,1]
	v_mov_b32_e32 v3, v24
	v_mov_b32_e32 v12, v25
	v_cvt_pk_fp8_f32 v11, v3, v12 op_sel:[0,0,1]
	global_store_dwordx2 v[6:7], v[8:9], off
	global_store_dwordx2 v[6:7], v[10:11], off offset:2048
	v_add_u32_e32 v9, 0x80, v2
	v_ashrrev_i32_e32 v10, 4, v9
	v_mov_b32_e32 v6, 0
	v_mov_b32_e32 v7, 0
	v_mov_b32_e32 v8, 0
	v_ashrrev_i32_e32 v11, 31, v10
	v_lshlrev_b64 v[10:11], 18, v[10:11]
	v_lshl_add_u64 v[10:11], s[24:25], 0, v[10:11]
	v_lshl_add_u64 v[10:11], v[10:11], 0, s[20:21]
	v_lshl_add_u64 v[10:11], v[10:11], 0, v[172:173]
	v_lshl_add_u64 v[10:11], v[10:11], 0, v[170:171]
; __device__ __forceinline__ unsigned pk4_fp8(float a, float b, float c, float d) {
;     a = fminf(fmaxf(a, -448.f), 448.f); b = fminf(fmaxf(b, -448.f), 448.f); c = fminf(fmaxf(c, -448.f), 448.f); d = fminf(fmaxf(d, -448.f), 448.f);
;     int w = 0; w = __builtin_amdgcn_cvt_pk_fp8_f32(a, b, w, false); w = __builtin_amdgcn_cvt_pk_fp8_f32(c, d, w, true); return (unsigned)w;
;     __device__ __forceinline__ void operator()(const f32x4 (&acc)[2][2][4][2], const Unit& u, int wr, int wc, int fr, int fq) const {
;     ...
;                 const int row = row0 + ai * HALF + m * 16;
;                 const float rs = rsqrtf(ss[row] * (1.0f / 4096.0f) + RMS_EPS) * (1.0f / 64.0f);
;                 unsigned char* rowp = U + ((size_t)(row >> 4) * 512 + (col0 >> 5)) * 512 + (row & 15) * 32 + (col0 & 31);
; #pragma unroll
;                 for (int bj = 0; bj < 2; ++bj) {
;                     f32x4 v0 = acc[ai][bj][m][0] * rs, v1 = acc[ai][bj][m][1] * rs;
; #pragma unroll
;                     for (int j = 0; j < 4; ++j) { const float a = fmaxf(v0[j], 0.f), b = fmaxf(v1[j], 0.f); v0[j] = a * a * 4.f; v1[j] = b * b * 4.f; }
;                     u32x2 w; w.x = pk4_fp8(v0[0], v0[1], v0[2], v0[3]); w.y = pk4_fp8(v1[0], v1[1], v1[2], v1[3]);
;                     *(u32x2*)(rowp + bj * (HALF / 32) * 512) = w;
	v_fmamk_f32 v3, v238, 0x39800000, v194
	v_mul_f32_e32 v9, 0x4b800000, v3
	v_cmp_gt_f32_e32 vcc, s43, v3
	s_nop 1
	v_cndmask_b32_e32 v3, v3, v9, vcc
	v_rsq_f32_e32 v3, v3
	s_nop 0
	v_mul_f32_e32 v9, 0x45800000, v3
	v_cndmask_b32_e32 v3, v3, v9, vcc
	v_mul_f32_e32 v12, 0x3d000000, v3
	v_pk_mul_f32 v[16:17], v[94:95], v[12:13] op_sel_hi:[1,0]
	v_pk_mul_f32 v[20:21], v[90:91], v[12:13] op_sel_hi:[1,0]
	v_pk_mul_f32 v[24:25], v[86:87], v[12:13] op_sel_hi:[1,0]
	v_pk_mul_f32 v[14:15], v[96:97], v[12:13] op_sel_hi:[1,0]
	v_pk_mul_f32 v[18:19], v[92:93], v[12:13] op_sel_hi:[1,0]
	v_pk_mul_f32 v[22:23], v[88:89], v[12:13] op_sel_hi:[1,0]
	v_pk_mul_f32 v[26:27], v[84:85], v[12:13] op_sel_hi:[1,0]
	v_pk_mul_f32 v[12:13], v[82:83], v[12:13] op_sel_hi:[1,0]
	v_med3_f32 v3, v16, 0, s99
	v_med3_f32 v9, v20, 0, s99
	v_med3_f32 v16, v17, 0, s99
	v_med3_f32 v17, v21, 0, s99
	v_med3_f32 v20, v24, 0, s99
	v_med3_f32 v21, v25, 0, s99
	v_med3_f32 v12, v12, 0, s99
	v_med3_f32 v13, v13, 0, s99
	v_mul_f32_e32 v3, v3, v3
	v_mul_f32_e32 v9, v9, v9
	v_mul_f32_e32 v16, v16, v16
	v_mul_f32_e32 v17, v17, v17
	v_mul_f32_e32 v20, v20, v20
	v_mul_f32_e32 v21, v21, v21
	v_mul_f32_e32 v12, v12, v12
	v_mul_f32_e32 v13, v13, v13
	v_med3_f32 v14, v14, 0, s99
	v_med3_f32 v18, v18, 0, s99
	v_med3_f32 v15, v15, 0, s99
	v_med3_f32 v19, v19, 0, s99
	v_med3_f32 v22, v22, 0, s99
	v_med3_f32 v23, v23, 0, s99
	v_cvt_pk_fp8_f32 v6, v3, v16
	v_cvt_pk_fp8_f32 v7, v9, v17
	v_cvt_pk_fp8_f32 v8, v20, v21
	v_mov_b32_e32 v9, 0
	v_med3_f32 v24, v26, 0, s99
	v_med3_f32 v25, v27, 0, s99
	v_mul_f32_e32 v14, v14, v14
	v_mul_f32_e32 v18, v18, v18
	v_mul_f32_e32 v15, v15, v15
	v_mul_f32_e32 v19, v19, v19
	v_mul_f32_e32 v22, v22, v22
	v_mul_f32_e32 v23, v23, v23
	v_cvt_pk_fp8_f32 v9, v12, v13
	v_mul_f32_e32 v24, v24, v24
	v_mul_f32_e32 v25, v25, v25
	v_mov_b32_e32 v3, v23
	v_cvt_pk_fp8_f32 v6, v14, v15 op_sel:[0,0,1]
	v_cvt_pk_fp8_f32 v7, v18, v19 op_sel:[0,0,1]
	v_cvt_pk_fp8_f32 v8, v22, v3 op_sel:[0,0,1]
	v_mov_b32_e32 v3, v24
	v_mov_b32_e32 v12, v25
	v_cvt_pk_fp8_f32 v9, v3, v12 op_sel:[0,0,1]
	global_store_dwordx2 v[10:11], v[6:7], off
	global_store_dwordx2 v[10:11], v[8:9], off offset:2048
	v_add_u32_e32 v9, 0x90, v2
	v_ashrrev_i32_e32 v10, 4, v9
	v_mov_b32_e32 v6, 0
	v_mov_b32_e32 v7, 0
	v_mov_b32_e32 v8, 0
	v_ashrrev_i32_e32 v11, 31, v10
	v_lshlrev_b64 v[10:11], 18, v[10:11]
	v_lshl_add_u64 v[10:11], s[24:25], 0, v[10:11]
	v_lshl_add_u64 v[10:11], v[10:11], 0, s[20:21]
	v_lshl_add_u64 v[10:11], v[10:11], 0, v[172:173]
	v_lshl_add_u64 v[10:11], v[10:11], 0, v[170:171]
	v_fmamk_f32 v3, v239, 0x39800000, v194
	v_mul_f32_e32 v9, 0x4b800000, v3
	v_cmp_gt_f32_e32 vcc, s43, v3
	s_nop 1
	v_cndmask_b32_e32 v3, v3, v9, vcc
	v_rsq_f32_e32 v3, v3
	s_nop 0
	v_mul_f32_e32 v9, 0x45800000, v3
	v_cndmask_b32_e32 v3, v3, v9, vcc
	v_mul_f32_e32 v12, 0x3d000000, v3
	v_pk_mul_f32 v[16:17], v[78:79], v[12:13] op_sel_hi:[1,0]
	v_pk_mul_f32 v[20:21], v[74:75], v[12:13] op_sel_hi:[1,0]
	v_pk_mul_f32 v[14:15], v[80:81], v[12:13] op_sel_hi:[1,0]
	v_pk_mul_f32 v[18:19], v[76:77], v[12:13] op_sel_hi:[1,0]
	v_pk_mul_f32 v[22:23], v[72:73], v[12:13] op_sel_hi:[1,0]
	v_pk_mul_f32 v[24:25], v[70:71], v[12:13] op_sel_hi:[1,0]
	v_pk_mul_f32 v[26:27], v[68:69], v[12:13] op_sel_hi:[1,0]
	v_pk_mul_f32 v[12:13], v[66:67], v[12:13] op_sel_hi:[1,0]
	v_med3_f32 v3, v16, 0, s99
	v_med3_f32 v9, v20, 0, s99
	v_med3_f32 v16, v17, 0, s99
	v_med3_f32 v17, v21, 0, s99
	v_med3_f32 v20, v24, 0, s99
	v_med3_f32 v12, v12, 0, s99
	v_med3_f32 v21, v25, 0, s99
	v_med3_f32 v13, v13, 0, s99
	v_mul_f32_e32 v3, v3, v3
	v_mul_f32_e32 v9, v9, v9
	v_mul_f32_e32 v16, v16, v16
	v_mul_f32_e32 v17, v17, v17
	v_mul_f32_e32 v20, v20, v20
	v_mul_f32_e32 v12, v12, v12
	v_mul_f32_e32 v21, v21, v21
	v_mul_f32_e32 v13, v13, v13
	v_med3_f32 v14, v14, 0, s99
	v_med3_f32 v18, v18, 0, s99
	v_med3_f32 v15, v15, 0, s99
	v_med3_f32 v19, v19, 0, s99
	v_cvt_pk_fp8_f32 v6, v3, v16
	v_cvt_pk_fp8_f32 v7, v9, v17
	v_mov_b32_e32 v3, v12
	v_mov_b32_e32 v12, v13
	v_mov_b32_e32 v9, 0
	v_med3_f32 v22, v22, 0, s99
	v_med3_f32 v24, v26, 0, s99
	v_med3_f32 v23, v23, 0, s99
	v_med3_f32 v25, v27, 0, s99
	v_mul_f32_e32 v14, v14, v14
	v_mul_f32_e32 v18, v18, v18
	v_mul_f32_e32 v15, v15, v15
	v_mul_f32_e32 v19, v19, v19
	v_cvt_pk_fp8_f32 v8, v20, v21
	v_cvt_pk_fp8_f32 v9, v3, v12
	v_mul_f32_e32 v22, v22, v22
	v_mul_f32_e32 v24, v24, v24
	v_mul_f32_e32 v23, v23, v23
	v_mul_f32_e32 v25, v25, v25
	v_cvt_pk_fp8_f32 v6, v14, v15 op_sel:[0,0,1]
	v_cvt_pk_fp8_f32 v7, v18, v19 op_sel:[0,0,1]
	v_mov_b32_e32 v3, v24
	v_mov_b32_e32 v12, v25
	v_cvt_pk_fp8_f32 v8, v22, v23 op_sel:[0,0,1]
	v_cvt_pk_fp8_f32 v9, v3, v12 op_sel:[0,0,1]
	global_store_dwordx2 v[10:11], v[6:7], off
	global_store_dwordx2 v[10:11], v[8:9], off offset:2048
	v_add_u32_e32 v9, 0xa0, v2
	v_ashrrev_i32_e32 v10, 4, v9
	v_mov_b32_e32 v6, 0
	v_mov_b32_e32 v7, 0
	v_mov_b32_e32 v8, 0
	v_ashrrev_i32_e32 v11, 31, v10
	v_lshlrev_b64 v[10:11], 18, v[10:11]
	v_lshl_add_u64 v[10:11], s[24:25], 0, v[10:11]
; __device__ __forceinline__ unsigned pk4_fp8(float a, float b, float c, float d) {
;     a = fminf(fmaxf(a, -448.f), 448.f); b = fminf(fmaxf(b, -448.f), 448.f); c = fminf(fmaxf(c, -448.f), 448.f); d = fminf(fmaxf(d, -448.f), 448.f);
;     int w = 0; w = __builtin_amdgcn_cvt_pk_fp8_f32(a, b, w, false); w = __builtin_amdgcn_cvt_pk_fp8_f32(c, d, w, true); return (unsigned)w;
;     __device__ __forceinline__ void operator()(const f32x4 (&acc)[2][2][4][2], const Unit& u, int wr, int wc, int fr, int fq) const {
;     ...
;                 const int row = row0 + ai * HALF + m * 16;
;                 const float rs = rsqrtf(ss[row] * (1.0f / 4096.0f) + RMS_EPS) * (1.0f / 64.0f);
;                 unsigned char* rowp = U + ((size_t)(row >> 4) * 512 + (col0 >> 5)) * 512 + (row & 15) * 32 + (col0 & 31);
; #pragma unroll
;                 for (int bj = 0; bj < 2; ++bj) {
;                     f32x4 v0 = acc[ai][bj][m][0] * rs, v1 = acc[ai][bj][m][1] * rs;
; #pragma unroll
;                     for (int j = 0; j < 4; ++j) { const float a = fmaxf(v0[j], 0.f), b = fmaxf(v1[j], 0.f); v0[j] = a * a * 4.f; v1[j] = b * b * 4.f; }
;                     u32x2 w; w.x = pk4_fp8(v0[0], v0[1], v0[2], v0[3]); w.y = pk4_fp8(v1[0], v1[1], v1[2], v1[3]);
;                     *(u32x2*)(rowp + bj * (HALF / 32) * 512) = w;
	v_lshl_add_u64 v[10:11], v[10:11], 0, s[20:21]
	v_lshl_add_u64 v[10:11], v[10:11], 0, v[172:173]
	v_lshl_add_u64 v[10:11], v[10:11], 0, v[170:171]
	v_add_u32_e32 v2, 0xb0, v2
	v_ashrrev_i32_e32 v2, 4, v2
	v_fmamk_f32 v3, v240, 0x39800000, v194
	v_mul_f32_e32 v9, 0x4b800000, v3
	v_cmp_gt_f32_e32 vcc, s43, v3
	s_nop 1
	v_cndmask_b32_e32 v3, v3, v9, vcc
	v_rsq_f32_e32 v3, v3
	s_nop 0
	v_mul_f32_e32 v9, 0x45800000, v3
	v_cndmask_b32_e32 v3, v3, v9, vcc
	v_mul_f32_e32 v12, 0x3d000000, v3
	v_pk_mul_f32 v[16:17], v[62:63], v[12:13] op_sel_hi:[1,0]
	v_pk_mul_f32 v[20:21], v[58:59], v[12:13] op_sel_hi:[1,0]
	v_pk_mul_f32 v[14:15], v[64:65], v[12:13] op_sel_hi:[1,0]
	v_pk_mul_f32 v[18:19], v[60:61], v[12:13] op_sel_hi:[1,0]
	v_pk_mul_f32 v[22:23], v[56:57], v[12:13] op_sel_hi:[1,0]
	v_pk_mul_f32 v[24:25], v[54:55], v[12:13] op_sel_hi:[1,0]
	v_pk_mul_f32 v[26:27], v[52:53], v[12:13] op_sel_hi:[1,0]
	v_pk_mul_f32 v[12:13], v[50:51], v[12:13] op_sel_hi:[1,0]
	v_med3_f32 v3, v16, 0, s99
	v_med3_f32 v9, v20, 0, s99
	v_med3_f32 v16, v17, 0, s99
	v_med3_f32 v17, v21, 0, s99
	v_med3_f32 v20, v24, 0, s99
	v_med3_f32 v12, v12, 0, s99
	v_med3_f32 v21, v25, 0, s99
	v_med3_f32 v13, v13, 0, s99
	v_mul_f32_e32 v3, v3, v3
	v_mul_f32_e32 v9, v9, v9
	v_mul_f32_e32 v16, v16, v16
	v_mul_f32_e32 v17, v17, v17
	v_mul_f32_e32 v20, v20, v20
	v_mul_f32_e32 v12, v12, v12
	v_mul_f32_e32 v21, v21, v21
	v_mul_f32_e32 v13, v13, v13
	v_med3_f32 v14, v14, 0, s99
	v_med3_f32 v18, v18, 0, s99
	v_med3_f32 v15, v15, 0, s99
	v_med3_f32 v19, v19, 0, s99
	v_cvt_pk_fp8_f32 v6, v3, v16
	v_cvt_pk_fp8_f32 v7, v9, v17
	v_mov_b32_e32 v3, v13
	v_mov_b32_e32 v9, 0
	v_med3_f32 v22, v22, 0, s99
	v_med3_f32 v24, v26, 0, s99
	v_med3_f32 v23, v23, 0, s99
	v_med3_f32 v25, v27, 0, s99
	v_mul_f32_e32 v14, v14, v14
	v_mul_f32_e32 v18, v18, v18
	v_mul_f32_e32 v15, v15, v15
	v_mul_f32_e32 v19, v19, v19
	v_cvt_pk_fp8_f32 v8, v20, v21
	v_cvt_pk_fp8_f32 v9, v12, v3
	v_mul_f32_e32 v22, v22, v22
	v_mul_f32_e32 v24, v24, v24
	v_mul_f32_e32 v23, v23, v23
	v_mul_f32_e32 v25, v25, v25
	v_cvt_pk_fp8_f32 v6, v14, v15 op_sel:[0,0,1]
	v_cvt_pk_fp8_f32 v7, v18, v19 op_sel:[0,0,1]
	v_mov_b32_e32 v3, v24
	v_mov_b32_e32 v12, v25
	v_cvt_pk_fp8_f32 v8, v22, v23 op_sel:[0,0,1]
	v_cvt_pk_fp8_f32 v9, v3, v12 op_sel:[0,0,1]
	global_store_dwordx2 v[10:11], v[6:7], off
	global_store_dwordx2 v[10:11], v[8:9], off offset:2048
	v_mov_b32_e32 v4, 0
	v_mov_b32_e32 v5, 0
	v_mov_b32_e32 v6, 0
	v_mov_b32_e32 v7, 0
	v_ashrrev_i32_e32 v3, 31, v2
	v_lshlrev_b64 v[2:3], 18, v[2:3]
	v_lshl_add_u64 v[2:3], s[24:25], 0, v[2:3]
	v_lshl_add_u64 v[2:3], v[2:3], 0, s[20:21]
	v_lshl_add_u64 v[2:3], v[2:3], 0, v[172:173]
	v_lshl_add_u64 v[2:3], v[2:3], 0, v[170:171]
	v_fmamk_f32 v8, v241, 0x39800000, v194
	v_mul_f32_e32 v9, 0x4b800000, v8
	v_cmp_gt_f32_e32 vcc, s43, v8
	s_nop 1
	v_cndmask_b32_e32 v8, v8, v9, vcc
	v_rsq_f32_e32 v8, v8
	s_nop 0
	v_mul_f32_e32 v9, 0x45800000, v8
	v_cndmask_b32_e32 v8, v8, v9, vcc
	v_mul_f32_e32 v8, 0x3d000000, v8
	v_pk_mul_f32 v[12:13], v[46:47], v[8:9] op_sel_hi:[1,0]
	v_pk_mul_f32 v[16:17], v[42:43], v[8:9] op_sel_hi:[1,0]
	v_pk_mul_f32 v[10:11], v[48:49], v[8:9] op_sel_hi:[1,0]
	v_pk_mul_f32 v[14:15], v[44:45], v[8:9] op_sel_hi:[1,0]
	v_pk_mul_f32 v[18:19], v[40:41], v[8:9] op_sel_hi:[1,0]
	v_pk_mul_f32 v[20:21], v[38:39], v[8:9] op_sel_hi:[1,0]
	v_pk_mul_f32 v[22:23], v[36:37], v[8:9] op_sel_hi:[1,0]
	v_pk_mul_f32 v[8:9], v[34:35], v[8:9] op_sel_hi:[1,0]
	v_med3_f32 v12, v12, 0, s99
	v_med3_f32 v16, v16, 0, s99
	v_med3_f32 v13, v13, 0, s99
	v_med3_f32 v17, v17, 0, s99
	v_med3_f32 v20, v20, 0, s99
	v_med3_f32 v8, v8, 0, s99
	v_med3_f32 v21, v21, 0, s99
	v_med3_f32 v9, v9, 0, s99
	v_mul_f32_e32 v12, v12, v12
	v_mul_f32_e32 v16, v16, v16
	v_mul_f32_e32 v13, v13, v13
	v_mul_f32_e32 v17, v17, v17
	v_mul_f32_e32 v20, v20, v20
	v_mul_f32_e32 v8, v8, v8
	v_mul_f32_e32 v21, v21, v21
	v_mul_f32_e32 v9, v9, v9
	v_med3_f32 v10, v10, 0, s99
	v_med3_f32 v14, v14, 0, s99
	v_med3_f32 v11, v11, 0, s99
	v_med3_f32 v15, v15, 0, s99
	v_cvt_pk_fp8_f32 v4, v12, v13
	v_cvt_pk_fp8_f32 v5, v16, v17
	v_med3_f32 v18, v18, 0, s99
	v_med3_f32 v22, v22, 0, s99
	v_med3_f32 v19, v19, 0, s99
	v_med3_f32 v23, v23, 0, s99
	v_mul_f32_e32 v10, v10, v10
	v_mul_f32_e32 v14, v14, v14
	v_mul_f32_e32 v11, v11, v11
	v_mul_f32_e32 v15, v15, v15
	v_cvt_pk_fp8_f32 v6, v20, v21
	v_cvt_pk_fp8_f32 v7, v8, v9
	v_mul_f32_e32 v18, v18, v18
	v_mul_f32_e32 v22, v22, v22
	v_mul_f32_e32 v19, v19, v19
	v_mul_f32_e32 v23, v23, v23
	v_cvt_pk_fp8_f32 v4, v10, v11 op_sel:[0,0,1]
	v_cvt_pk_fp8_f32 v5, v14, v15 op_sel:[0,0,1]
	v_mov_b32_e32 v8, v22
	v_mov_b32_e32 v9, v23
	v_cvt_pk_fp8_f32 v6, v18, v19 op_sel:[0,0,1]
	v_cvt_pk_fp8_f32 v7, v8, v9 op_sel:[0,0,1]
	s_andn2_b64 vcc, exec, s[0:1]
	s_mov_b64 s[0:1], -1
	global_store_dwordx2 v[2:3], v[4:5], off
	global_store_dwordx2 v[2:3], v[6:7], off offset:2048
	s_cbranch_vccnz .LBB0_2273
	s_andn2_b64 vcc, exec, s[4:5]
	s_cbranch_vccnz .LBB0_2272
	s_barrier
	s_branch .LBB0_2272
